# HGRN2 pass A: the 64 per-unit v_cndmask selects for the own sub-chunk removed (fj[jo] = exp(0) = 1.0 exactly, the product already equals qe)
# speedup vs baseline: 1.0192x; 1.0009x over previous
; __device__ __forceinline__ unsigned pk2(float lo, float hi) { f32x2_t v = {lo, hi}; bf16x2_t b = __builtin_convertvector(v, bf16x2_t); return __builtin_bit_cast(unsigned, b); }
; #define LAS __attribute__((address_space(3)))
; __device__ __forceinline__ int qj_row0(int j) { return (j == 0) ? 0 : (j == 1) ? 64 : (j == 2) ? 112 : 144; }
; template <bool DRY> __device__ __forceinline__ void pass_a_all(LAS unsigned char* lds, bf16_t* PROJ, const bf16_t* __restrict__ KK, bf16_t* HST, float* HD, int u0, int ustep, int uend) {
;     ...
;         float E[4][2], pre[2] = {0.f, 0.f};
;         { float s0 = 0.f, s1 = 0.f;
; #pragma unroll
;           for (int sgi = 0; sgi < 8; ++sgi) { const f32x2_t v = *(const LAS f32x2_t*)(segt + sgi * 128 + 2 * kp); if (sgi < sg8) { pre[0] += v.x; pre[1] += v.y; } s0 += v.x; s1 += v.y; if (sgi & 1) { E[sgi >> 1][0] = s0; E[sgi >> 1][1] = s1; } } }
;         const int jo = sg8 >> 1;
;         float Eown[2];
; #pragma unroll
;         for (int k2 = 0; k2 < 2; ++k2) Eown[k2] = (jo == 0) ? E[0][k2] : (jo == 1) ? E[1][k2] : (jo == 2) ? E[2][k2] : E[3][k2];
;         {
;             bf16_t* pq = PROJ + (row0 + 8 * sg8) * NPROJ + C_HQ + h * 128 + 2 * kp;
;             unsigned kt[2][4];
;             float fj[4][2], f0[2], f3[2];
; #pragma unroll
;             for (int k2 = 0; k2 < 2; ++k2) { f0[k2] = __expf(Eown[k2]); f3[k2] = __expf(E[3][k2] - Eown[k2]);
; #pragma unroll
;                 for (int j = 0; j < 4; ++j) fj[j][k2] = __expf(Eown[k2] - E[j][k2]); }
; #pragma unroll
;             for (int i = 0; i < 8; ++i) {
;                 const int t = 8 * sg8 + i;
;                 float qe[2], ke1[2];
; #pragma unroll
;                 for (int k2 = 0; k2 < 2; ++k2) { const float A = pre[k2] + Aa[i][k2]; const float e1 = __expf(A - Eown[k2]), r1 = __builtin_amdgcn_rcpf(e1);
;                     qe[k2] = qv[i][k2] * e1; ke1[k2] = kv[i][k2] * r1; }
;                 if (!DRY) *(unsigned*)(pq + (size_t)i * NPROJ) = pk2(qe[0] * f0[0], qe[1] * f0[1]);
; #pragma unroll
;                 for (int j = 0; j < 4; ++j) if (j <= jo) *(LAS unsigned*)(lds + L_QJ + (qj_row0(j) + t - 16 * j) * P272 + kp * 4) = (j == jo) ? pk2(qe[0], qe[1]) : pk2(qe[0] * fj[j][0], qe[1] * fj[j][1]);
;                 *(LAS unsigned*)(lds + L_KH + t * P272 + kp * 4) = pk2(ke1[0], ke1[1]);
.LBB0_484:
	v_cndmask_b32_e64 v105, 0, v105, s[10:11]
	v_cndmask_b32_e64 v104, 0, v104, s[10:11]
	v_pk_add_f32 v[16:17], v[16:17], v[104:105]
	s_ashr_i32 s34, s40, 8
	v_cndmask_b32_e64 v17, v105, v17, s[12:13]
	v_cndmask_b32_e64 v16, v104, v16, s[12:13]
	v_pk_add_f32 v[10:11], v[10:11], v[16:17]
	s_ashr_i32 s35, s34, 31
	v_cndmask_b32_e64 v11, v17, v11, s[14:15]
	v_cndmask_b32_e64 v10, v16, v10, s[14:15]
	v_pk_add_f32 v[12:13], v[12:13], v[10:11]
	s_add_i32 s36, s67, s48
	v_cndmask_b32_e64 v11, v11, v13, s[16:17]
	v_cndmask_b32_e64 v10, v10, v12, s[16:17]
	v_pk_add_f32 v[6:7], v[6:7], v[10:11]
	s_and_b32 s36, s36, 0xfc0
	v_cndmask_b32_e64 v7, v11, v7, s[18:19]
	v_cndmask_b32_e64 v6, v10, v6, s[18:19]
	v_pk_add_f32 v[8:9], v[8:9], v[6:7]
	s_lshl_b64 s[46:47], s[34:35], 12
	v_cndmask_b32_e64 v7, v7, v9, s[20:21]
	v_cndmask_b32_e64 v6, v6, v8, s[20:21]
	v_pk_add_f32 v[2:3], v[2:3], v[6:7]
	s_or_b32 s46, s46, s36
	v_cndmask_b32_e64 v3, v7, v3, s[22:23]
	v_cndmask_b32_e64 v2, v6, v2, s[22:23]
	v_pk_add_f32 v[4:5], v[4:5], v[2:3]
	s_add_u32 s34, s46, s33
	v_cndmask_b32_e64 v5, v3, v5, s[24:25]
	v_cndmask_b32_e64 v4, v2, v4, s[24:25]
	v_mul_f32_e32 v3, 0x3fb8aa3b, v106
	v_pk_add_f32 v[8:9], v[76:77], v[4:5]
	v_exp_f32_e32 v7, v3
	v_sub_f32_e32 v3, v8, v57
	v_mul_f32_e32 v3, 0x3fb8aa3b, v3
	v_readlane_b32 s35, v254, 37
	v_exp_f32_e32 v8, v3
	v_sub_f32_e32 v3, v9, v106
	s_addc_u32 s35, s47, s35
	v_mul_f32_e32 v3, 0x3fb8aa3b, v3
	s_mulk_i32 s35, 0x1c00
	s_mul_hi_u32 s36, s34, 0x1c00
	v_mul_f32_e32 v2, 0x3fb8aa3b, v57
	v_exp_f32_e32 v9, v3
	s_add_i32 s36, s36, s35
	s_mulk_i32 s34, 0x1c00
	v_exp_f32_e32 v6, v2
	s_add_u32 s34, s56, s34
	v_sub_f32_e32 v2, v57, v102
	v_sub_f32_e32 v3, v106, v103
	v_lshlrev_b32_e32 v108, 16, v74
	v_and_b32_e32 v109, 0xffff0000, v74
	s_addc_u32 s35, s57, s36
	s_add_i32 s36, s61, s63
	v_mul_f32_e32 v2, 0x3fb8aa3b, v2
	v_mul_f32_e32 v3, 0x3fb8aa3b, v3
	s_and_b32 s36, s36, 0x180
	v_exp_f32_e32 v2, v2
	v_exp_f32_e32 v3, v3
	v_pk_mul_f32 v[76:77], v[8:9], v[108:109]
	s_lshl_b32 s68, s36, 1
	v_pk_mul_f32 v[10:11], v[6:7], v[76:77]
	s_add_u32 s54, s34, s68
	v_cvt_pk_bf16_f32 v10, v10, v11
	v_cndmask_b32_e64 v11, 0, 1, s[74:75]
	s_addc_u32 s55, s35, 0
	v_cmp_ne_u32_e64 s[34:35], 1, v11
	s_andn2_b64 vcc, exec, s[74:75]
	global_store_dword v44, v10, s[54:55] offset:3072
	s_cbranch_vccnz .LBB0_486
	v_pk_mul_f32 v[10:11], v[2:3], v[76:77]
	s_nop 0
	v_cvt_pk_bf16_f32 v10, v10, v11
	ds_write_b32 v147, v10 offset:2048
.LBB0_486:
	v_sub_f32_e32 v10, v57, v98
	v_sub_f32_e32 v11, v106, v99
	v_mul_f32_e32 v10, 0x3fb8aa3b, v10
	v_mul_f32_e32 v11, 0x3fb8aa3b, v11
	v_exp_f32_e32 v10, v10
	v_exp_f32_e32 v11, v11
	v_cndmask_b32_e64 v12, 0, 1, s[76:77]
	v_cmp_ne_u32_e64 s[36:37], 1, v12
	s_andn2_b64 vcc, exec, s[76:77]
	s_cbranch_vccnz .LBB0_488
	v_pk_mul_f32 v[12:13], v[10:11], v[76:77]
	s_nop 0
	v_cvt_pk_bf16_f32 v12, v12, v13
	ds_write_b32 v147, v12 offset:15104
.LBB0_488:
	v_sub_f32_e32 v12, v57, v96
	v_sub_f32_e32 v13, v106, v97
	v_mul_f32_e32 v12, 0x3fb8aa3b, v12
	v_mul_f32_e32 v13, 0x3fb8aa3b, v13
	v_exp_f32_e32 v12, v12
	v_exp_f32_e32 v13, v13
	v_cndmask_b32_e64 v16, 0, 1, s[78:79]
	v_cmp_ne_u32_e64 s[38:39], 1, v16
	s_andn2_b64 vcc, exec, s[78:79]
	s_cbranch_vccnz .LBB0_490
	v_pk_mul_f32 v[16:17], v[12:13], v[76:77]
	s_nop 0
	v_cvt_pk_bf16_f32 v16, v16, v17
	ds_write_b32 v147, v16 offset:23808
.LBB0_490:
	v_sub_f32_e32 v16, v57, v14
	v_sub_f32_e32 v17, v106, v15
	v_mul_f32_e32 v16, 0x3fb8aa3b, v16
	v_mul_f32_e32 v17, 0x3fb8aa3b, v17
	v_exp_f32_e32 v16, v16
	v_exp_f32_e32 v17, v17
	v_cndmask_b32_e64 v74, 0, 1, s[80:81]
	v_cmp_ne_u32_e64 s[40:41], 1, v74
	s_andn2_b64 vcc, exec, s[80:81]
	s_cbranch_vccnz .LBB0_492
	v_pk_mul_f32 v[96:97], v[16:17], v[76:77]
	s_nop 0
	v_cvt_pk_bf16_f32 v74, v96, v97
	ds_write_b32 v147, v74 offset:28160
.LBB0_492:
	v_pk_add_f32 v[92:93], v[92:93], v[4:5]
	v_rcp_f32_e32 v8, v8
	v_sub_f32_e32 v92, v92, v57
	v_sub_f32_e32 v93, v93, v106
	v_rcp_f32_e32 v9, v9
	v_mul_f32_e32 v92, 0x3fb8aa3b, v92
	v_mul_f32_e32 v93, 0x3fb8aa3b, v93
	v_exp_f32_e32 v92, v92
	v_exp_f32_e32 v93, v93
	v_pk_add_f32 v[96:97], v[100:101], 1.0 op_sel_hi:[1,0] neg_lo:[1,0] neg_hi:[1,0]
	v_lshlrev_b32_e32 v74, 16, v75
	v_pk_mul_f32 v[8:9], v[96:97], v[8:9]
	v_and_b32_e32 v75, 0xffff0000, v75
	v_lshl_add_u64 v[76:77], s[54:55], 0, v[44:45]
	s_mov_b64 s[54:55], 0xc00
	v_cvt_pk_bf16_f32 v96, v8, v9
	v_pk_mul_f32 v[74:75], v[92:93], v[74:75]
	v_lshl_add_u64 v[76:77], v[76:77], 0, s[54:55]
	ds_write_b32 v147, v96 offset:45568
	v_pk_mul_f32 v[96:97], v[6:7], v[74:75]
	s_nop 0
	v_cvt_pk_bf16_f32 v98, v96, v97
	v_add_co_u32_e32 v96, vcc, 0x1000, v76
	s_nop 1
	v_addc_co_u32_e32 v97, vcc, 0, v77, vcc
	s_and_b64 vcc, exec, s[34:35]
	global_store_dword v[96:97], v98, off offset:3072
	s_cbranch_vccnz .LBB0_496
	v_pk_mul_f32 v[96:97], v[2:3], v[74:75]
	s_nop 0
	v_cvt_pk_bf16_f32 v96, v96, v97
	ds_write_b32 v147, v96 offset:2320
	s_and_b64 vcc, exec, s[36:37]
	s_cbranch_vccz .LBB0_497

; __device__ __forceinline__ unsigned pk2(float lo, float hi) { f32x2_t v = {lo, hi}; bf16x2_t b = __builtin_convertvector(v, bf16x2_t); return __builtin_bit_cast(unsigned, b); }
; #define LAS __attribute__((address_space(3)))
; __device__ __forceinline__ int qj_row0(int j) { return (j == 0) ? 0 : (j == 1) ? 64 : (j == 2) ? 112 : 144; }
; template <bool DRY> __device__ __forceinline__ void pass_a_all(LAS unsigned char* lds, bf16_t* PROJ, const bf16_t* __restrict__ KK, bf16_t* HST, float* HD, int u0, int ustep, int uend) {
;     ...
;                 if (!DRY) *(unsigned*)(pq + (size_t)i * NPROJ) = pk2(qe[0] * f0[0], qe[1] * f0[1]);
; #pragma unroll
;                 for (int j = 0; j < 4; ++j) if (j <= jo) *(LAS unsigned*)(lds + L_QJ + (qj_row0(j) + t - 16 * j) * P272 + kp * 4) = (j == jo) ? pk2(qe[0], qe[1]) : pk2(qe[0] * fj[j][0], qe[1] * fj[j][1]);
;                 *(LAS unsigned*)(lds + L_KH + t * P272 + kp * 4) = pk2(ke1[0], ke1[1]);
.LBB0_495:
	v_pk_mul_f32 v[96:97], v[12:13], v[74:75]
	s_nop 0
	v_cvt_pk_bf16_f32 v96, v96, v97
	ds_write_b32 v147, v96 offset:24080
	s_and_b64 vcc, exec, s[40:41]
	s_cbranch_vccz .LBB0_499
	s_branch .LBB0_500

; __device__ __forceinline__ unsigned pk2(float lo, float hi) { f32x2_t v = {lo, hi}; bf16x2_t b = __builtin_convertvector(v, bf16x2_t); return __builtin_bit_cast(unsigned, b); }
; #define LAS __attribute__((address_space(3)))
; __device__ __forceinline__ int qj_row0(int j) { return (j == 0) ? 0 : (j == 1) ? 64 : (j == 2) ? 112 : 144; }
; template <bool DRY> __device__ __forceinline__ void pass_a_all(LAS unsigned char* lds, bf16_t* PROJ, const bf16_t* __restrict__ KK, bf16_t* HST, float* HD, int u0, int ustep, int uend) {
;     ...
;                 if (!DRY) *(unsigned*)(pq + (size_t)i * NPROJ) = pk2(qe[0] * f0[0], qe[1] * f0[1]);
; #pragma unroll
;                 for (int j = 0; j < 4; ++j) if (j <= jo) *(LAS unsigned*)(lds + L_QJ + (qj_row0(j) + t - 16 * j) * P272 + kp * 4) = (j == jo) ? pk2(qe[0], qe[1]) : pk2(qe[0] * fj[j][0], qe[1] * fj[j][1]);
;                 *(LAS unsigned*)(lds + L_KH + t * P272 + kp * 4) = pk2(ke1[0], ke1[1]);
.LBB0_497:
	v_pk_mul_f32 v[96:97], v[10:11], v[74:75]
	s_nop 0
	v_cvt_pk_bf16_f32 v96, v96, v97
	ds_write_b32 v147, v96 offset:15376
	s_and_b64 vcc, exec, s[38:39]
	s_cbranch_vccz .LBB0_495

; __device__ __forceinline__ unsigned pk2(float lo, float hi) { f32x2_t v = {lo, hi}; bf16x2_t b = __builtin_convertvector(v, bf16x2_t); return __builtin_bit_cast(unsigned, b); }
; #define LAS __attribute__((address_space(3)))
; __device__ __forceinline__ int qj_row0(int j) { return (j == 0) ? 0 : (j == 1) ? 64 : (j == 2) ? 112 : 144; }
; template <bool DRY> __device__ __forceinline__ void pass_a_all(LAS unsigned char* lds, bf16_t* PROJ, const bf16_t* __restrict__ KK, bf16_t* HST, float* HD, int u0, int ustep, int uend) {
;     ...
;             for (int i = 0; i < 8; ++i) {
;                 const int t = 8 * sg8 + i;
;                 float qe[2], ke1[2];
; #pragma unroll
;                 for (int k2 = 0; k2 < 2; ++k2) { const float A = pre[k2] + Aa[i][k2]; const float e1 = __expf(A - Eown[k2]), r1 = __builtin_amdgcn_rcpf(e1);
;                     qe[k2] = qv[i][k2] * e1; ke1[k2] = kv[i][k2] * r1; }
;                 if (!DRY) *(unsigned*)(pq + (size_t)i * NPROJ) = pk2(qe[0] * f0[0], qe[1] * f0[1]);
; #pragma unroll
;                 for (int j = 0; j < 4; ++j) if (j <= jo) *(LAS unsigned*)(lds + L_QJ + (qj_row0(j) + t - 16 * j) * P272 + kp * 4) = (j == jo) ? pk2(qe[0], qe[1]) : pk2(qe[0] * fj[j][0], qe[1] * fj[j][1]);
;                 *(LAS unsigned*)(lds + L_KH + t * P272 + kp * 4) = pk2(ke1[0], ke1[1]);
.LBB0_499:
	v_pk_mul_f32 v[96:97], v[16:17], v[74:75]
	s_nop 0
	v_cvt_pk_bf16_f32 v74, v96, v97
	ds_write_b32 v147, v74 offset:28432
.LBB0_500:
	v_pk_add_f32 v[86:87], v[86:87], v[4:5]
	v_rcp_f32_e32 v74, v92
	v_sub_f32_e32 v86, v86, v57
	v_sub_f32_e32 v87, v87, v106
	v_mul_f32_e32 v86, 0x3fb8aa3b, v86
	v_mul_f32_e32 v87, 0x3fb8aa3b, v87
	v_rcp_f32_e32 v75, v93
	v_exp_f32_e32 v86, v86
	v_exp_f32_e32 v87, v87
	v_pk_add_f32 v[92:93], v[94:95], 1.0 op_sel_hi:[1,0] neg_lo:[1,0] neg_hi:[1,0]
	v_lshlrev_b32_e32 v94, 16, v82
	v_and_b32_e32 v95, 0xffff0000, v82
	v_pk_mul_f32 v[74:75], v[92:93], v[74:75]
	v_pk_mul_f32 v[92:93], v[86:87], v[94:95]
	v_cvt_pk_bf16_f32 v82, v74, v75
	v_pk_mul_f32 v[94:95], v[6:7], v[92:93]
	ds_write_b32 v147, v82 offset:45840
	v_cvt_pk_bf16_f32 v82, v94, v95
	v_add_co_u32_e32 v94, vcc, 0x3000, v76
	s_nop 1
	v_addc_co_u32_e32 v95, vcc, 0, v77, vcc
	s_and_b64 vcc, exec, s[34:35]
	global_store_dword v[94:95], v82, off offset:2048
	s_cbranch_vccnz .LBB0_504
	v_pk_mul_f32 v[94:95], v[2:3], v[92:93]
	s_nop 0
	v_cvt_pk_bf16_f32 v82, v94, v95
	ds_write_b32 v147, v82 offset:2592
	s_and_b64 vcc, exec, s[36:37]
	s_cbranch_vccz .LBB0_505

; __device__ __forceinline__ unsigned pk2(float lo, float hi) { f32x2_t v = {lo, hi}; bf16x2_t b = __builtin_convertvector(v, bf16x2_t); return __builtin_bit_cast(unsigned, b); }
; #define LAS __attribute__((address_space(3)))
; __device__ __forceinline__ int qj_row0(int j) { return (j == 0) ? 0 : (j == 1) ? 64 : (j == 2) ? 112 : 144; }
; template <bool DRY> __device__ __forceinline__ void pass_a_all(LAS unsigned char* lds, bf16_t* PROJ, const bf16_t* __restrict__ KK, bf16_t* HST, float* HD, int u0, int ustep, int uend) {
;     ...
;                 if (!DRY) *(unsigned*)(pq + (size_t)i * NPROJ) = pk2(qe[0] * f0[0], qe[1] * f0[1]);
; #pragma unroll
;                 for (int j = 0; j < 4; ++j) if (j <= jo) *(LAS unsigned*)(lds + L_QJ + (qj_row0(j) + t - 16 * j) * P272 + kp * 4) = (j == jo) ? pk2(qe[0], qe[1]) : pk2(qe[0] * fj[j][0], qe[1] * fj[j][1]);
;                 *(LAS unsigned*)(lds + L_KH + t * P272 + kp * 4) = pk2(ke1[0], ke1[1]);
.LBB0_503:
	v_pk_mul_f32 v[94:95], v[12:13], v[92:93]
	s_nop 0
	v_cvt_pk_bf16_f32 v82, v94, v95
	ds_write_b32 v147, v82 offset:24352
	s_and_b64 vcc, exec, s[40:41]
	s_cbranch_vccz .LBB0_507
	s_branch .LBB0_508

; __device__ __forceinline__ unsigned pk2(float lo, float hi) { f32x2_t v = {lo, hi}; bf16x2_t b = __builtin_convertvector(v, bf16x2_t); return __builtin_bit_cast(unsigned, b); }
; #define LAS __attribute__((address_space(3)))
; __device__ __forceinline__ int qj_row0(int j) { return (j == 0) ? 0 : (j == 1) ? 64 : (j == 2) ? 112 : 144; }
; template <bool DRY> __device__ __forceinline__ void pass_a_all(LAS unsigned char* lds, bf16_t* PROJ, const bf16_t* __restrict__ KK, bf16_t* HST, float* HD, int u0, int ustep, int uend) {
;     ...
;                 if (!DRY) *(unsigned*)(pq + (size_t)i * NPROJ) = pk2(qe[0] * f0[0], qe[1] * f0[1]);
; #pragma unroll
;                 for (int j = 0; j < 4; ++j) if (j <= jo) *(LAS unsigned*)(lds + L_QJ + (qj_row0(j) + t - 16 * j) * P272 + kp * 4) = (j == jo) ? pk2(qe[0], qe[1]) : pk2(qe[0] * fj[j][0], qe[1] * fj[j][1]);
;                 *(LAS unsigned*)(lds + L_KH + t * P272 + kp * 4) = pk2(ke1[0], ke1[1]);
.LBB0_505:
	v_pk_mul_f32 v[94:95], v[10:11], v[92:93]
	s_nop 0
	v_cvt_pk_bf16_f32 v82, v94, v95
	ds_write_b32 v147, v82 offset:15648
	s_and_b64 vcc, exec, s[38:39]
	s_cbranch_vccz .LBB0_503

; __device__ __forceinline__ unsigned pk2(float lo, float hi) { f32x2_t v = {lo, hi}; bf16x2_t b = __builtin_convertvector(v, bf16x2_t); return __builtin_bit_cast(unsigned, b); }
; #define LAS __attribute__((address_space(3)))
; __device__ __forceinline__ int qj_row0(int j) { return (j == 0) ? 0 : (j == 1) ? 64 : (j == 2) ? 112 : 144; }
; template <bool DRY> __device__ __forceinline__ void pass_a_all(LAS unsigned char* lds, bf16_t* PROJ, const bf16_t* __restrict__ KK, bf16_t* HST, float* HD, int u0, int ustep, int uend) {
;     ...
;             for (int i = 0; i < 8; ++i) {
;                 const int t = 8 * sg8 + i;
;                 float qe[2], ke1[2];
; #pragma unroll
;                 for (int k2 = 0; k2 < 2; ++k2) { const float A = pre[k2] + Aa[i][k2]; const float e1 = __expf(A - Eown[k2]), r1 = __builtin_amdgcn_rcpf(e1);
;                     qe[k2] = qv[i][k2] * e1; ke1[k2] = kv[i][k2] * r1; }
;                 if (!DRY) *(unsigned*)(pq + (size_t)i * NPROJ) = pk2(qe[0] * f0[0], qe[1] * f0[1]);
; #pragma unroll
;                 for (int j = 0; j < 4; ++j) if (j <= jo) *(LAS unsigned*)(lds + L_QJ + (qj_row0(j) + t - 16 * j) * P272 + kp * 4) = (j == jo) ? pk2(qe[0], qe[1]) : pk2(qe[0] * fj[j][0], qe[1] * fj[j][1]);
;                 *(LAS unsigned*)(lds + L_KH + t * P272 + kp * 4) = pk2(ke1[0], ke1[1]);
.LBB0_507:
	v_pk_mul_f32 v[94:95], v[16:17], v[92:93]
	s_nop 0
	v_cvt_pk_bf16_f32 v82, v94, v95
	ds_write_b32 v147, v82 offset:28704
.LBB0_508:
	v_pk_add_f32 v[84:85], v[84:85], v[4:5]
	v_rcp_f32_e32 v86, v86
	v_sub_f32_e32 v84, v84, v57
	v_sub_f32_e32 v85, v85, v106
	v_rcp_f32_e32 v87, v87
	v_mul_f32_e32 v84, 0x3fb8aa3b, v84
	v_mul_f32_e32 v85, 0x3fb8aa3b, v85
	v_exp_f32_e32 v84, v84
	v_exp_f32_e32 v85, v85
	v_pk_add_f32 v[90:91], v[90:91], 1.0 op_sel_hi:[1,0] neg_lo:[1,0] neg_hi:[1,0]
	v_lshlrev_b32_e32 v82, 16, v83
	v_pk_mul_f32 v[86:87], v[90:91], v[86:87]
	v_and_b32_e32 v83, 0xffff0000, v83
	v_cvt_pk_bf16_f32 v90, v86, v87
	v_pk_mul_f32 v[82:83], v[84:85], v[82:83]
	ds_write_b32 v147, v90 offset:46112
	v_pk_mul_f32 v[90:91], v[6:7], v[82:83]
	s_nop 0
	v_cvt_pk_bf16_f32 v92, v90, v91
	v_add_co_u32_e32 v90, vcc, 0x5000, v76
	s_nop 1
	v_addc_co_u32_e32 v91, vcc, 0, v77, vcc
	s_and_b64 vcc, exec, s[34:35]
	global_store_dword v[90:91], v92, off offset:1024
	s_cbranch_vccnz .LBB0_512
	v_pk_mul_f32 v[90:91], v[2:3], v[82:83]
	s_nop 0
	v_cvt_pk_bf16_f32 v90, v90, v91
	ds_write_b32 v147, v90 offset:2864
	s_and_b64 vcc, exec, s[36:37]
	s_cbranch_vccz .LBB0_513

; __device__ __forceinline__ unsigned pk2(float lo, float hi) { f32x2_t v = {lo, hi}; bf16x2_t b = __builtin_convertvector(v, bf16x2_t); return __builtin_bit_cast(unsigned, b); }
; #define LAS __attribute__((address_space(3)))
; __device__ __forceinline__ int qj_row0(int j) { return (j == 0) ? 0 : (j == 1) ? 64 : (j == 2) ? 112 : 144; }
; template <bool DRY> __device__ __forceinline__ void pass_a_all(LAS unsigned char* lds, bf16_t* PROJ, const bf16_t* __restrict__ KK, bf16_t* HST, float* HD, int u0, int ustep, int uend) {
;     ...
;                 if (!DRY) *(unsigned*)(pq + (size_t)i * NPROJ) = pk2(qe[0] * f0[0], qe[1] * f0[1]);
; #pragma unroll
;                 for (int j = 0; j < 4; ++j) if (j <= jo) *(LAS unsigned*)(lds + L_QJ + (qj_row0(j) + t - 16 * j) * P272 + kp * 4) = (j == jo) ? pk2(qe[0], qe[1]) : pk2(qe[0] * fj[j][0], qe[1] * fj[j][1]);
;                 *(LAS unsigned*)(lds + L_KH + t * P272 + kp * 4) = pk2(ke1[0], ke1[1]);
.LBB0_511:
	v_pk_mul_f32 v[90:91], v[12:13], v[82:83]
	s_nop 0
	v_cvt_pk_bf16_f32 v90, v90, v91
	ds_write_b32 v147, v90 offset:24624
	s_and_b64 vcc, exec, s[40:41]
	s_cbranch_vccz .LBB0_515
	s_branch .LBB0_516

; __device__ __forceinline__ unsigned pk2(float lo, float hi) { f32x2_t v = {lo, hi}; bf16x2_t b = __builtin_convertvector(v, bf16x2_t); return __builtin_bit_cast(unsigned, b); }
; #define LAS __attribute__((address_space(3)))
; __device__ __forceinline__ int qj_row0(int j) { return (j == 0) ? 0 : (j == 1) ? 64 : (j == 2) ? 112 : 144; }
; template <bool DRY> __device__ __forceinline__ void pass_a_all(LAS unsigned char* lds, bf16_t* PROJ, const bf16_t* __restrict__ KK, bf16_t* HST, float* HD, int u0, int ustep, int uend) {
;     ...
;                 if (!DRY) *(unsigned*)(pq + (size_t)i * NPROJ) = pk2(qe[0] * f0[0], qe[1] * f0[1]);
; #pragma unroll
;                 for (int j = 0; j < 4; ++j) if (j <= jo) *(LAS unsigned*)(lds + L_QJ + (qj_row0(j) + t - 16 * j) * P272 + kp * 4) = (j == jo) ? pk2(qe[0], qe[1]) : pk2(qe[0] * fj[j][0], qe[1] * fj[j][1]);
;                 *(LAS unsigned*)(lds + L_KH + t * P272 + kp * 4) = pk2(ke1[0], ke1[1]);
.LBB0_513:
	v_pk_mul_f32 v[90:91], v[10:11], v[82:83]
	s_nop 0
	v_cvt_pk_bf16_f32 v90, v90, v91
	ds_write_b32 v147, v90 offset:15920
	s_and_b64 vcc, exec, s[38:39]
	s_cbranch_vccz .LBB0_511

; __device__ __forceinline__ unsigned pk2(float lo, float hi) { f32x2_t v = {lo, hi}; bf16x2_t b = __builtin_convertvector(v, bf16x2_t); return __builtin_bit_cast(unsigned, b); }
; #define LAS __attribute__((address_space(3)))
; __device__ __forceinline__ int qj_row0(int j) { return (j == 0) ? 0 : (j == 1) ? 64 : (j == 2) ? 112 : 144; }
; template <bool DRY> __device__ __forceinline__ void pass_a_all(LAS unsigned char* lds, bf16_t* PROJ, const bf16_t* __restrict__ KK, bf16_t* HST, float* HD, int u0, int ustep, int uend) {
;     ...
;             for (int i = 0; i < 8; ++i) {
;                 const int t = 8 * sg8 + i;
;                 float qe[2], ke1[2];
; #pragma unroll
;                 for (int k2 = 0; k2 < 2; ++k2) { const float A = pre[k2] + Aa[i][k2]; const float e1 = __expf(A - Eown[k2]), r1 = __builtin_amdgcn_rcpf(e1);
;                     qe[k2] = qv[i][k2] * e1; ke1[k2] = kv[i][k2] * r1; }
;                 if (!DRY) *(unsigned*)(pq + (size_t)i * NPROJ) = pk2(qe[0] * f0[0], qe[1] * f0[1]);
; #pragma unroll
;                 for (int j = 0; j < 4; ++j) if (j <= jo) *(LAS unsigned*)(lds + L_QJ + (qj_row0(j) + t - 16 * j) * P272 + kp * 4) = (j == jo) ? pk2(qe[0], qe[1]) : pk2(qe[0] * fj[j][0], qe[1] * fj[j][1]);
;                 *(LAS unsigned*)(lds + L_KH + t * P272 + kp * 4) = pk2(ke1[0], ke1[1]);
.LBB0_515:
	v_pk_mul_f32 v[90:91], v[16:17], v[82:83]
	s_nop 0
	v_cvt_pk_bf16_f32 v82, v90, v91
	ds_write_b32 v147, v82 offset:28976
.LBB0_516:
	v_pk_add_f32 v[78:79], v[78:79], v[4:5]
	v_rcp_f32_e32 v82, v84
	v_sub_f32_e32 v78, v78, v57
	v_sub_f32_e32 v79, v79, v106
	v_mul_f32_e32 v78, 0x3fb8aa3b, v78
	v_mul_f32_e32 v79, 0x3fb8aa3b, v79
	v_rcp_f32_e32 v83, v85
	v_exp_f32_e32 v78, v78
	v_exp_f32_e32 v79, v79
	v_pk_add_f32 v[84:85], v[88:89], 1.0 op_sel_hi:[1,0] neg_lo:[1,0] neg_hi:[1,0]
	v_lshlrev_b32_e32 v88, 16, v68
	v_and_b32_e32 v89, 0xffff0000, v68
	v_pk_mul_f32 v[82:83], v[84:85], v[82:83]
	v_pk_mul_f32 v[84:85], v[78:79], v[88:89]
	v_cvt_pk_bf16_f32 v68, v82, v83
	v_pk_mul_f32 v[88:89], v[6:7], v[84:85]
	ds_write_b32 v147, v68 offset:46384
	v_cvt_pk_bf16_f32 v68, v88, v89
	v_add_co_u32_e32 v88, vcc, 0x7000, v76
	s_nop 1
	v_addc_co_u32_e32 v89, vcc, 0, v77, vcc
	s_and_b64 vcc, exec, s[34:35]
	global_store_dword v[88:89], v68, off
	s_cbranch_vccnz .LBB0_520
	v_pk_mul_f32 v[88:89], v[2:3], v[84:85]
	s_nop 0
	v_cvt_pk_bf16_f32 v68, v88, v89
	ds_write_b32 v147, v68 offset:3136
	s_and_b64 vcc, exec, s[36:37]
	s_cbranch_vccz .LBB0_521

; __device__ __forceinline__ unsigned pk2(float lo, float hi) { f32x2_t v = {lo, hi}; bf16x2_t b = __builtin_convertvector(v, bf16x2_t); return __builtin_bit_cast(unsigned, b); }
; #define LAS __attribute__((address_space(3)))
; __device__ __forceinline__ int qj_row0(int j) { return (j == 0) ? 0 : (j == 1) ? 64 : (j == 2) ? 112 : 144; }
; template <bool DRY> __device__ __forceinline__ void pass_a_all(LAS unsigned char* lds, bf16_t* PROJ, const bf16_t* __restrict__ KK, bf16_t* HST, float* HD, int u0, int ustep, int uend) {
;     ...
;                 if (!DRY) *(unsigned*)(pq + (size_t)i * NPROJ) = pk2(qe[0] * f0[0], qe[1] * f0[1]);
; #pragma unroll
;                 for (int j = 0; j < 4; ++j) if (j <= jo) *(LAS unsigned*)(lds + L_QJ + (qj_row0(j) + t - 16 * j) * P272 + kp * 4) = (j == jo) ? pk2(qe[0], qe[1]) : pk2(qe[0] * fj[j][0], qe[1] * fj[j][1]);
;                 *(LAS unsigned*)(lds + L_KH + t * P272 + kp * 4) = pk2(ke1[0], ke1[1]);
.LBB0_519:
	v_pk_mul_f32 v[88:89], v[12:13], v[84:85]
	s_nop 0
	v_cvt_pk_bf16_f32 v68, v88, v89
	ds_write_b32 v147, v68 offset:24896
	s_and_b64 vcc, exec, s[40:41]
	s_cbranch_vccz .LBB0_523
	s_branch .LBB0_524

; __device__ __forceinline__ unsigned pk2(float lo, float hi) { f32x2_t v = {lo, hi}; bf16x2_t b = __builtin_convertvector(v, bf16x2_t); return __builtin_bit_cast(unsigned, b); }
; #define LAS __attribute__((address_space(3)))
; __device__ __forceinline__ int qj_row0(int j) { return (j == 0) ? 0 : (j == 1) ? 64 : (j == 2) ? 112 : 144; }
; template <bool DRY> __device__ __forceinline__ void pass_a_all(LAS unsigned char* lds, bf16_t* PROJ, const bf16_t* __restrict__ KK, bf16_t* HST, float* HD, int u0, int ustep, int uend) {
;     ...
;                 if (!DRY) *(unsigned*)(pq + (size_t)i * NPROJ) = pk2(qe[0] * f0[0], qe[1] * f0[1]);
; #pragma unroll
;                 for (int j = 0; j < 4; ++j) if (j <= jo) *(LAS unsigned*)(lds + L_QJ + (qj_row0(j) + t - 16 * j) * P272 + kp * 4) = (j == jo) ? pk2(qe[0], qe[1]) : pk2(qe[0] * fj[j][0], qe[1] * fj[j][1]);
;                 *(LAS unsigned*)(lds + L_KH + t * P272 + kp * 4) = pk2(ke1[0], ke1[1]);
.LBB0_521:
	v_pk_mul_f32 v[88:89], v[10:11], v[84:85]
	s_nop 0
	v_cvt_pk_bf16_f32 v68, v88, v89
	ds_write_b32 v147, v68 offset:16192
	s_and_b64 vcc, exec, s[38:39]
	s_cbranch_vccz .LBB0_519

; __device__ __forceinline__ unsigned pk2(float lo, float hi) { f32x2_t v = {lo, hi}; bf16x2_t b = __builtin_convertvector(v, bf16x2_t); return __builtin_bit_cast(unsigned, b); }
; #define LAS __attribute__((address_space(3)))
; __device__ __forceinline__ int qj_row0(int j) { return (j == 0) ? 0 : (j == 1) ? 64 : (j == 2) ? 112 : 144; }
; template <bool DRY> __device__ __forceinline__ void pass_a_all(LAS unsigned char* lds, bf16_t* PROJ, const bf16_t* __restrict__ KK, bf16_t* HST, float* HD, int u0, int ustep, int uend) {
;     ...
;             for (int i = 0; i < 8; ++i) {
;                 const int t = 8 * sg8 + i;
;                 float qe[2], ke1[2];
; #pragma unroll
;                 for (int k2 = 0; k2 < 2; ++k2) { const float A = pre[k2] + Aa[i][k2]; const float e1 = __expf(A - Eown[k2]), r1 = __builtin_amdgcn_rcpf(e1);
;                     qe[k2] = qv[i][k2] * e1; ke1[k2] = kv[i][k2] * r1; }
;                 if (!DRY) *(unsigned*)(pq + (size_t)i * NPROJ) = pk2(qe[0] * f0[0], qe[1] * f0[1]);
; #pragma unroll
;                 for (int j = 0; j < 4; ++j) if (j <= jo) *(LAS unsigned*)(lds + L_QJ + (qj_row0(j) + t - 16 * j) * P272 + kp * 4) = (j == jo) ? pk2(qe[0], qe[1]) : pk2(qe[0] * fj[j][0], qe[1] * fj[j][1]);
;                 *(LAS unsigned*)(lds + L_KH + t * P272 + kp * 4) = pk2(ke1[0], ke1[1]);
.LBB0_523:
	v_pk_mul_f32 v[88:89], v[16:17], v[84:85]
	s_nop 0
	v_cvt_pk_bf16_f32 v68, v88, v89
	ds_write_b32 v147, v68 offset:29248
.LBB0_524:
	v_pk_add_f32 v[70:71], v[70:71], v[4:5]
	v_rcp_f32_e32 v78, v78
	v_sub_f32_e32 v70, v70, v57
	v_sub_f32_e32 v71, v71, v106
	v_rcp_f32_e32 v79, v79
	v_mul_f32_e32 v70, 0x3fb8aa3b, v70
	v_mul_f32_e32 v71, 0x3fb8aa3b, v71
	v_exp_f32_e32 v70, v70
	v_exp_f32_e32 v71, v71
	v_pk_add_f32 v[80:81], v[80:81], 1.0 op_sel_hi:[1,0] neg_lo:[1,0] neg_hi:[1,0]
	v_lshlrev_b32_e32 v68, 16, v69
	v_pk_mul_f32 v[78:79], v[80:81], v[78:79]
	v_and_b32_e32 v69, 0xffff0000, v69
	v_cvt_pk_bf16_f32 v80, v78, v79
	v_pk_mul_f32 v[68:69], v[70:71], v[68:69]
	ds_write_b32 v147, v80 offset:46656
	v_pk_mul_f32 v[80:81], v[6:7], v[68:69]
	s_nop 0
	v_cvt_pk_bf16_f32 v84, v80, v81
	v_add_co_u32_e32 v80, vcc, 0x8000, v76
	s_nop 1
	v_addc_co_u32_e32 v81, vcc, 0, v77, vcc
	s_and_b64 vcc, exec, s[34:35]
	global_store_dword v[80:81], v84, off offset:3072
	s_cbranch_vccnz .LBB0_528
	v_pk_mul_f32 v[80:81], v[2:3], v[68:69]
	s_nop 0
	v_cvt_pk_bf16_f32 v80, v80, v81
	ds_write_b32 v147, v80 offset:3408
	s_and_b64 vcc, exec, s[36:37]
	s_cbranch_vccz .LBB0_529

; __device__ __forceinline__ unsigned pk2(float lo, float hi) { f32x2_t v = {lo, hi}; bf16x2_t b = __builtin_convertvector(v, bf16x2_t); return __builtin_bit_cast(unsigned, b); }
; #define LAS __attribute__((address_space(3)))
; __device__ __forceinline__ int qj_row0(int j) { return (j == 0) ? 0 : (j == 1) ? 64 : (j == 2) ? 112 : 144; }
; template <bool DRY> __device__ __forceinline__ void pass_a_all(LAS unsigned char* lds, bf16_t* PROJ, const bf16_t* __restrict__ KK, bf16_t* HST, float* HD, int u0, int ustep, int uend) {
;     ...
;                 if (!DRY) *(unsigned*)(pq + (size_t)i * NPROJ) = pk2(qe[0] * f0[0], qe[1] * f0[1]);
; #pragma unroll
;                 for (int j = 0; j < 4; ++j) if (j <= jo) *(LAS unsigned*)(lds + L_QJ + (qj_row0(j) + t - 16 * j) * P272 + kp * 4) = (j == jo) ? pk2(qe[0], qe[1]) : pk2(qe[0] * fj[j][0], qe[1] * fj[j][1]);
;                 *(LAS unsigned*)(lds + L_KH + t * P272 + kp * 4) = pk2(ke1[0], ke1[1]);
.LBB0_527:
	v_pk_mul_f32 v[80:81], v[12:13], v[68:69]
	s_nop 0
	v_cvt_pk_bf16_f32 v80, v80, v81
	ds_write_b32 v147, v80 offset:25168
	s_and_b64 vcc, exec, s[40:41]
	s_cbranch_vccz .LBB0_531
	s_branch .LBB0_532

; __device__ __forceinline__ unsigned pk2(float lo, float hi) { f32x2_t v = {lo, hi}; bf16x2_t b = __builtin_convertvector(v, bf16x2_t); return __builtin_bit_cast(unsigned, b); }
; #define LAS __attribute__((address_space(3)))
; __device__ __forceinline__ int qj_row0(int j) { return (j == 0) ? 0 : (j == 1) ? 64 : (j == 2) ? 112 : 144; }
; template <bool DRY> __device__ __forceinline__ void pass_a_all(LAS unsigned char* lds, bf16_t* PROJ, const bf16_t* __restrict__ KK, bf16_t* HST, float* HD, int u0, int ustep, int uend) {
;     ...
;                 if (!DRY) *(unsigned*)(pq + (size_t)i * NPROJ) = pk2(qe[0] * f0[0], qe[1] * f0[1]);
; #pragma unroll
;                 for (int j = 0; j < 4; ++j) if (j <= jo) *(LAS unsigned*)(lds + L_QJ + (qj_row0(j) + t - 16 * j) * P272 + kp * 4) = (j == jo) ? pk2(qe[0], qe[1]) : pk2(qe[0] * fj[j][0], qe[1] * fj[j][1]);
;                 *(LAS unsigned*)(lds + L_KH + t * P272 + kp * 4) = pk2(ke1[0], ke1[1]);
.LBB0_529:
	v_pk_mul_f32 v[80:81], v[10:11], v[68:69]
	s_nop 0
	v_cvt_pk_bf16_f32 v80, v80, v81
	ds_write_b32 v147, v80 offset:16464
	s_and_b64 vcc, exec, s[38:39]
	s_cbranch_vccz .LBB0_527

; __device__ __forceinline__ unsigned pk2(float lo, float hi) { f32x2_t v = {lo, hi}; bf16x2_t b = __builtin_convertvector(v, bf16x2_t); return __builtin_bit_cast(unsigned, b); }
; #define LAS __attribute__((address_space(3)))
; __device__ __forceinline__ int qj_row0(int j) { return (j == 0) ? 0 : (j == 1) ? 64 : (j == 2) ? 112 : 144; }
; template <bool DRY> __device__ __forceinline__ void pass_a_all(LAS unsigned char* lds, bf16_t* PROJ, const bf16_t* __restrict__ KK, bf16_t* HST, float* HD, int u0, int ustep, int uend) {
;     ...
;             for (int i = 0; i < 8; ++i) {
;                 const int t = 8 * sg8 + i;
;                 float qe[2], ke1[2];
; #pragma unroll
;                 for (int k2 = 0; k2 < 2; ++k2) { const float A = pre[k2] + Aa[i][k2]; const float e1 = __expf(A - Eown[k2]), r1 = __builtin_amdgcn_rcpf(e1);
;                     qe[k2] = qv[i][k2] * e1; ke1[k2] = kv[i][k2] * r1; }
;                 if (!DRY) *(unsigned*)(pq + (size_t)i * NPROJ) = pk2(qe[0] * f0[0], qe[1] * f0[1]);
; #pragma unroll
;                 for (int j = 0; j < 4; ++j) if (j <= jo) *(LAS unsigned*)(lds + L_QJ + (qj_row0(j) + t - 16 * j) * P272 + kp * 4) = (j == jo) ? pk2(qe[0], qe[1]) : pk2(qe[0] * fj[j][0], qe[1] * fj[j][1]);
;                 *(LAS unsigned*)(lds + L_KH + t * P272 + kp * 4) = pk2(ke1[0], ke1[1]);
.LBB0_531:
	v_pk_mul_f32 v[80:81], v[16:17], v[68:69]
	s_nop 0
	v_cvt_pk_bf16_f32 v68, v80, v81
	ds_write_b32 v147, v68 offset:29520
.LBB0_532:
	v_pk_add_f32 v[64:65], v[64:65], v[4:5]
	v_rcp_f32_e32 v68, v70
	v_sub_f32_e32 v64, v64, v57
	v_sub_f32_e32 v65, v65, v106
	v_mul_f32_e32 v64, 0x3fb8aa3b, v64
	v_mul_f32_e32 v65, 0x3fb8aa3b, v65
	v_rcp_f32_e32 v69, v71
	v_exp_f32_e32 v64, v64
	v_exp_f32_e32 v65, v65
	v_pk_add_f32 v[70:71], v[72:73], 1.0 op_sel_hi:[1,0] neg_lo:[1,0] neg_hi:[1,0]
	v_lshlrev_b32_e32 v72, 16, v58
	v_and_b32_e32 v73, 0xffff0000, v58
	v_pk_mul_f32 v[68:69], v[70:71], v[68:69]
	v_pk_mul_f32 v[70:71], v[64:65], v[72:73]
	v_cvt_pk_bf16_f32 v58, v68, v69
	v_pk_mul_f32 v[72:73], v[6:7], v[70:71]
	ds_write_b32 v147, v58 offset:46928
	v_cvt_pk_bf16_f32 v58, v72, v73
	v_add_co_u32_e32 v72, vcc, 0xa000, v76
	s_nop 1
	v_addc_co_u32_e32 v73, vcc, 0, v77, vcc
	s_and_b64 vcc, exec, s[34:35]
	global_store_dword v[72:73], v58, off offset:2048
	s_cbranch_vccnz .LBB0_536
	v_pk_mul_f32 v[72:73], v[2:3], v[70:71]
	s_nop 0
	v_cvt_pk_bf16_f32 v58, v72, v73
	ds_write_b32 v147, v58 offset:3680
	s_and_b64 vcc, exec, s[36:37]
	s_cbranch_vccz .LBB0_537

; __device__ __forceinline__ unsigned pk2(float lo, float hi) { f32x2_t v = {lo, hi}; bf16x2_t b = __builtin_convertvector(v, bf16x2_t); return __builtin_bit_cast(unsigned, b); }
; #define LAS __attribute__((address_space(3)))
; __device__ __forceinline__ int qj_row0(int j) { return (j == 0) ? 0 : (j == 1) ? 64 : (j == 2) ? 112 : 144; }
; template <bool DRY> __device__ __forceinline__ void pass_a_all(LAS unsigned char* lds, bf16_t* PROJ, const bf16_t* __restrict__ KK, bf16_t* HST, float* HD, int u0, int ustep, int uend) {
;     ...
;                 if (!DRY) *(unsigned*)(pq + (size_t)i * NPROJ) = pk2(qe[0] * f0[0], qe[1] * f0[1]);
; #pragma unroll
;                 for (int j = 0; j < 4; ++j) if (j <= jo) *(LAS unsigned*)(lds + L_QJ + (qj_row0(j) + t - 16 * j) * P272 + kp * 4) = (j == jo) ? pk2(qe[0], qe[1]) : pk2(qe[0] * fj[j][0], qe[1] * fj[j][1]);
;                 *(LAS unsigned*)(lds + L_KH + t * P272 + kp * 4) = pk2(ke1[0], ke1[1]);
.LBB0_535:
	v_pk_mul_f32 v[72:73], v[12:13], v[70:71]
	s_nop 0
	v_cvt_pk_bf16_f32 v58, v72, v73
	ds_write_b32 v147, v58 offset:25440
	s_and_b64 vcc, exec, s[40:41]
	s_cbranch_vccz .LBB0_539
	s_branch .LBB0_540

; __device__ __forceinline__ unsigned pk2(float lo, float hi) { f32x2_t v = {lo, hi}; bf16x2_t b = __builtin_convertvector(v, bf16x2_t); return __builtin_bit_cast(unsigned, b); }
; #define LAS __attribute__((address_space(3)))
; __device__ __forceinline__ int qj_row0(int j) { return (j == 0) ? 0 : (j == 1) ? 64 : (j == 2) ? 112 : 144; }
; template <bool DRY> __device__ __forceinline__ void pass_a_all(LAS unsigned char* lds, bf16_t* PROJ, const bf16_t* __restrict__ KK, bf16_t* HST, float* HD, int u0, int ustep, int uend) {
;     ...
;                 if (!DRY) *(unsigned*)(pq + (size_t)i * NPROJ) = pk2(qe[0] * f0[0], qe[1] * f0[1]);
; #pragma unroll
;                 for (int j = 0; j < 4; ++j) if (j <= jo) *(LAS unsigned*)(lds + L_QJ + (qj_row0(j) + t - 16 * j) * P272 + kp * 4) = (j == jo) ? pk2(qe[0], qe[1]) : pk2(qe[0] * fj[j][0], qe[1] * fj[j][1]);
;                 *(LAS unsigned*)(lds + L_KH + t * P272 + kp * 4) = pk2(ke1[0], ke1[1]);
.LBB0_537:
	v_pk_mul_f32 v[72:73], v[10:11], v[70:71]
	s_nop 0
	v_cvt_pk_bf16_f32 v58, v72, v73
	ds_write_b32 v147, v58 offset:16736
	s_and_b64 vcc, exec, s[38:39]
	s_cbranch_vccz .LBB0_535

; __device__ __forceinline__ unsigned pk2(float lo, float hi) { f32x2_t v = {lo, hi}; bf16x2_t b = __builtin_convertvector(v, bf16x2_t); return __builtin_bit_cast(unsigned, b); }
; #define LAS __attribute__((address_space(3)))
; __device__ __forceinline__ int qj_row0(int j) { return (j == 0) ? 0 : (j == 1) ? 64 : (j == 2) ? 112 : 144; }
; template <bool DRY> __device__ __forceinline__ void pass_a_all(LAS unsigned char* lds, bf16_t* PROJ, const bf16_t* __restrict__ KK, bf16_t* HST, float* HD, int u0, int ustep, int uend) {
;     ...
;             for (int i = 0; i < 8; ++i) {
;                 const int t = 8 * sg8 + i;
;                 float qe[2], ke1[2];
; #pragma unroll
;                 for (int k2 = 0; k2 < 2; ++k2) { const float A = pre[k2] + Aa[i][k2]; const float e1 = __expf(A - Eown[k2]), r1 = __builtin_amdgcn_rcpf(e1);
;                     qe[k2] = qv[i][k2] * e1; ke1[k2] = kv[i][k2] * r1; }
;                 if (!DRY) *(unsigned*)(pq + (size_t)i * NPROJ) = pk2(qe[0] * f0[0], qe[1] * f0[1]);
; #pragma unroll
;                 for (int j = 0; j < 4; ++j) if (j <= jo) *(LAS unsigned*)(lds + L_QJ + (qj_row0(j) + t - 16 * j) * P272 + kp * 4) = (j == jo) ? pk2(qe[0], qe[1]) : pk2(qe[0] * fj[j][0], qe[1] * fj[j][1]);
;                 *(LAS unsigned*)(lds + L_KH + t * P272 + kp * 4) = pk2(ke1[0], ke1[1]);
.LBB0_539:
	v_pk_mul_f32 v[72:73], v[16:17], v[70:71]
	s_nop 0
	v_cvt_pk_bf16_f32 v58, v72, v73
	ds_write_b32 v147, v58 offset:29792
.LBB0_540:
	v_pk_add_f32 v[4:5], v[60:61], v[4:5]
	v_rcp_f32_e32 v64, v64
	v_sub_f32_e32 v4, v4, v57
	v_sub_f32_e32 v5, v5, v106
	v_mul_f32_e32 v4, 0x3fb8aa3b, v4
	v_mul_f32_e32 v5, 0x3fb8aa3b, v5
	v_rcp_f32_e32 v65, v65
	v_exp_f32_e32 v4, v4
	v_exp_f32_e32 v5, v5
	v_pk_add_f32 v[66:67], v[66:67], 1.0 op_sel_hi:[1,0] neg_lo:[1,0] neg_hi:[1,0]
	v_lshlrev_b32_e32 v58, 16, v59
	v_and_b32_e32 v59, 0xffff0000, v59
	v_pk_mul_f32 v[64:65], v[66:67], v[64:65]
	v_pk_mul_f32 v[58:59], v[4:5], v[58:59]
	v_cvt_pk_bf16_f32 v60, v64, v65
	v_pk_mul_f32 v[6:7], v[6:7], v[58:59]
	ds_write_b32 v147, v60 offset:47200
	v_cvt_pk_bf16_f32 v60, v6, v7
	v_add_co_u32_e32 v6, vcc, 0xc000, v76
	s_nop 1
	v_addc_co_u32_e32 v7, vcc, 0, v77, vcc
	s_and_b64 vcc, exec, s[34:35]
	global_store_dword v[6:7], v60, off offset:1024
	s_cbranch_vccnz .LBB0_544
	v_pk_mul_f32 v[2:3], v[2:3], v[58:59]
	s_nop 0
	v_cvt_pk_bf16_f32 v2, v2, v3
	ds_write_b32 v147, v2 offset:3952
	s_and_b64 vcc, exec, s[36:37]
	s_cbranch_vccz .LBB0_545

; __device__ __forceinline__ unsigned pk2(float lo, float hi) { f32x2_t v = {lo, hi}; bf16x2_t b = __builtin_convertvector(v, bf16x2_t); return __builtin_bit_cast(unsigned, b); }
; #define LAS __attribute__((address_space(3)))
; __device__ __forceinline__ int qj_row0(int j) { return (j == 0) ? 0 : (j == 1) ? 64 : (j == 2) ? 112 : 144; }
; template <bool DRY> __device__ __forceinline__ void pass_a_all(LAS unsigned char* lds, bf16_t* PROJ, const bf16_t* __restrict__ KK, bf16_t* HST, float* HD, int u0, int ustep, int uend) {
;     ...
;                 if (!DRY) *(unsigned*)(pq + (size_t)i * NPROJ) = pk2(qe[0] * f0[0], qe[1] * f0[1]);
; #pragma unroll
;                 for (int j = 0; j < 4; ++j) if (j <= jo) *(LAS unsigned*)(lds + L_QJ + (qj_row0(j) + t - 16 * j) * P272 + kp * 4) = (j == jo) ? pk2(qe[0], qe[1]) : pk2(qe[0] * fj[j][0], qe[1] * fj[j][1]);
;                 *(LAS unsigned*)(lds + L_KH + t * P272 + kp * 4) = pk2(ke1[0], ke1[1]);
.LBB0_543:
	v_pk_mul_f32 v[2:3], v[12:13], v[58:59]
	s_nop 0
	v_cvt_pk_bf16_f32 v2, v2, v3
	ds_write_b32 v147, v2 offset:25712
	s_and_b64 vcc, exec, s[40:41]
	s_cbranch_vccz .LBB0_547
	s_branch .LBB0_548

; __device__ __forceinline__ unsigned pk2(float lo, float hi) { f32x2_t v = {lo, hi}; bf16x2_t b = __builtin_convertvector(v, bf16x2_t); return __builtin_bit_cast(unsigned, b); }
; #define LAS __attribute__((address_space(3)))
; __device__ __forceinline__ int qj_row0(int j) { return (j == 0) ? 0 : (j == 1) ? 64 : (j == 2) ? 112 : 144; }
; template <bool DRY> __device__ __forceinline__ void pass_a_all(LAS unsigned char* lds, bf16_t* PROJ, const bf16_t* __restrict__ KK, bf16_t* HST, float* HD, int u0, int ustep, int uend) {
;     ...
;                 if (!DRY) *(unsigned*)(pq + (size_t)i * NPROJ) = pk2(qe[0] * f0[0], qe[1] * f0[1]);
; #pragma unroll
;                 for (int j = 0; j < 4; ++j) if (j <= jo) *(LAS unsigned*)(lds + L_QJ + (qj_row0(j) + t - 16 * j) * P272 + kp * 4) = (j == jo) ? pk2(qe[0], qe[1]) : pk2(qe[0] * fj[j][0], qe[1] * fj[j][1]);
;                 *(LAS unsigned*)(lds + L_KH + t * P272 + kp * 4) = pk2(ke1[0], ke1[1]);
.LBB0_545:
	v_pk_mul_f32 v[2:3], v[10:11], v[58:59]
	s_nop 0
	v_cvt_pk_bf16_f32 v2, v2, v3
	ds_write_b32 v147, v2 offset:17008
	s_and_b64 vcc, exec, s[38:39]
	s_cbranch_vccz .LBB0_543

; __device__ __forceinline__ unsigned pk2(float lo, float hi) { f32x2_t v = {lo, hi}; bf16x2_t b = __builtin_convertvector(v, bf16x2_t); return __builtin_bit_cast(unsigned, b); }
; #define LAS __attribute__((address_space(3)))
; __device__ __forceinline__ int qj_row0(int j) { return (j == 0) ? 0 : (j == 1) ? 64 : (j == 2) ? 112 : 144; }
; template <bool DRY> __device__ __forceinline__ void pass_a_all(LAS unsigned char* lds, bf16_t* PROJ, const bf16_t* __restrict__ KK, bf16_t* HST, float* HD, int u0, int ustep, int uend) {
;     ...
;                 if (!DRY) *(unsigned*)(pq + (size_t)i * NPROJ) = pk2(qe[0] * f0[0], qe[1] * f0[1]);
; #pragma unroll
;                 for (int j = 0; j < 4; ++j) if (j <= jo) *(LAS unsigned*)(lds + L_QJ + (qj_row0(j) + t - 16 * j) * P272 + kp * 4) = (j == jo) ? pk2(qe[0], qe[1]) : pk2(qe[0] * fj[j][0], qe[1] * fj[j][1]);
;                 *(LAS unsigned*)(lds + L_KH + t * P272 + kp * 4) = pk2(ke1[0], ke1[1]);
.LBB0_547:
	v_pk_mul_f32 v[2:3], v[16:17], v[58:59]
	s_nop 0
	v_cvt_pk_bf16_f32 v2, v2, v3
	ds_write_b32 v147, v2 offset:30064
